# PEER u side: expert-row pieces requested with four neighbouring lanes contiguous (row = lane >> 2) and moved into the MFMA fragment lanes by ds_bpermute; was 64 separate 16-byte requests per load
# speedup vs baseline: 1.0236x; 1.0236x over previous
.LBB0_1535:
	v_lshl_or_b32 v7, v7, 11, v50
	v_lshrrev_b32_e32 v8, 15, v7
	v_and_b32_e32 v8, 0x1fffc, v8
	s_add_i32 s0, 0, 0x20500
	v_add_u32_e32 v8, s0, v8
	s_waitcnt lgkmcnt(0)
	s_barrier
	ds_read_b32 v8, v8
	v_add_u32_e32 v58, 0x200, v50
	v_lshlrev_b32_e32 v5, 2, v5
	v_lshl_or_b32 v6, v6, 11, v58
	v_add_u32_e32 v57, 0x400, v50
	s_waitcnt lgkmcnt(0)
	v_lshlrev_b32_e32 v8, 2, v8
	v_add3_u32 v5, s35, v8, v5
	ds_write_b32 v5, v7
	v_lshrrev_b32_e32 v5, 15, v6
	v_and_b32_e32 v5, 0x1fffc, v5
	v_add_u32_e32 v5, s0, v5
	ds_read_b32 v5, v5
	v_lshlrev_b32_e32 v3, 2, v3
	v_lshl_or_b32 v4, v4, 11, v57
	v_add_u32_e32 v55, 0x600, v50
	v_lshlrev_b32_e32 v1, 2, v1
	s_waitcnt lgkmcnt(0)
	v_lshlrev_b32_e32 v5, 2, v5
	v_add3_u32 v3, s35, v5, v3
	ds_write_b32 v3, v6
	v_lshrrev_b32_e32 v3, 15, v4
	v_and_b32_e32 v3, 0x1fffc, v3
	v_add_u32_e32 v3, s0, v3
	ds_read_b32 v3, v3
	v_lshl_or_b32 v2, v2, 11, v55
	v_lshlrev_b32_e32 v0, 2, v0
	v_and_b32_e32 v61, -16, v145
	v_add_u32_e32 v32, s20, v61
	s_waitcnt lgkmcnt(0)
	v_lshlrev_b32_e32 v3, 2, v3
	v_add3_u32 v1, s35, v3, v1
	ds_write_b32 v1, v4
	v_lshrrev_b32_e32 v1, 15, v2
	v_and_b32_e32 v1, 0x1fffc, v1
	v_add_u32_e32 v1, s0, v1
	ds_read_b32 v1, v1
	v_and_b32_e32 v3, 15, v145
	v_lshlrev_b32_e32 v34, 2, v3
	v_readlane_b32 s0, v242, 31
	v_readlane_b32 s1, v242, 32
	s_waitcnt lgkmcnt(0)
	v_lshlrev_b32_e32 v1, 2, v1
	v_add3_u32 v0, s35, v1, v0
	ds_write_b32 v0, v2
	v_add_u32_e32 v2, s35, v34
	s_waitcnt lgkmcnt(0)
	s_barrier
	v_and_b32_e32 v161, 15, v145
	v_and_b32_e32 v162, -16, v145
	v_mov_b32_e32 v157, 0
	v_lshl_add_u32 v155, v161, 2, s35
	v_add_u32_e32 v156, s20, v162
	v_add_u32_e32 v154, s21, v162
	v_lshl_add_u64 v[152:153], s[0:1], 0, v[156:157]
	v_lshrrev_b32_e32 v170, 2, v145
	v_lshl_add_u32 v170, v170, 2, s35
	v_and_b32_e32 v174, 3, v145
	v_lshl_add_u32 v174, v174, 4, s20
	v_mov_b32_e32 v175, 0
	v_lshl_add_u64 v[172:173], s[0:1], 0, v[174:175]
	v_lshrrev_b32_e32 v171, 4, v145
	v_lshl_add_u32 v171, v161, 2, v171
	v_lshlrev_b32_e32 v171, 2, v171
	ds_read_b32 v182, v155
	ds_read_b32 v166, v170
	ds_read_b32 v183, v155 offset:64
	ds_read_b32 v167, v170 offset:64
	ds_read_b32 v184, v155 offset:128
	ds_read_b32 v168, v170 offset:128
	v_and_b32_e32 v163, 1, v145
	v_cmp_ne_u32_e64 s[2:3], 0, v163
	v_and_b32_e32 v163, 2, v145
	v_cmp_ne_u32_e64 s[10:11], 0, v163
	v_lshrrev_b32_e32 v163, 4, v145
	v_bfe_u32 v164, v145, 2, 2
	v_cmp_eq_u32_e64 s[12:13], v163, v164
	s_mov_b32 s50, 0x1c100
	v_mov_b32_e32 v230, 0
	v_mov_b32_e32 v231, 0
	v_mov_b32_e32 v232, 0
	v_mov_b32_e32 v233, 0
	v_mov_b32_e32 v148, 0
	v_mov_b32_e32 v150, 0
	v_mov_b32_e32 v234, 0
	v_mov_b32_e32 v235, 0
	v_mov_b32_e32 v236, 0
	v_mov_b32_e32 v237, 0
	v_mov_b32_e32 v149, 0
	v_mov_b32_e32 v151, 0
	s_waitcnt lgkmcnt(4)
	v_and_b32_e32 v174, 0xfffff800, v166
	v_lshl_add_u64 v[176:177], v[172:173], 0, v[174:175]
	global_load_dwordx4 v[0:3], v[176:177], off
	global_load_dwordx4 v[4:7], v[176:177], off offset:64
	global_load_dwordx4 v[8:11], v[176:177], off offset:128
	global_load_dwordx4 v[12:15], v[176:177], off offset:192
	s_waitcnt lgkmcnt(2)
	v_and_b32_e32 v174, 0xfffff800, v167
	v_lshl_add_u64 v[176:177], v[172:173], 0, v[174:175]
	global_load_dwordx4 v[16:19], v[176:177], off
	global_load_dwordx4 v[20:23], v[176:177], off offset:64
	global_load_dwordx4 v[24:27], v[176:177], off offset:128
	global_load_dwordx4 v[28:31], v[176:177], off offset:192
	s_waitcnt lgkmcnt(0)
	v_and_b32_e32 v174, 0xfffff800, v168
	v_lshl_add_u64 v[176:177], v[172:173], 0, v[174:175]
	global_load_dwordx4 v[32:35], v[176:177], off
	global_load_dwordx4 v[36:39], v[176:177], off offset:64
	global_load_dwordx4 v[40:43], v[176:177], off offset:128
	global_load_dwordx4 v[44:47], v[176:177], off offset:192
	s_mov_b32 s9, 0
.Lpu_loop:
	ds_read_b32 v185, v155 offset:192
	ds_read_b32 v169, v170 offset:192
	v_bfe_u32 v146, v182, 7, 4
	v_and_b32_e32 v148, 0x7ff, v182
	v_mad_u32_u24 v160, v146, s31, v154
	v_lshl_add_u32 v164, v146, 5, s16
	ds_read_b128 v[190:193], v160
	ds_read_b128 v[194:197], v160 offset:64
	ds_read_b128 v[198:201], v160 offset:128
	ds_read_b128 v[202:205], v160 offset:192
	ds_read_b128 v[206:209], v160 offset:256
	ds_read_b128 v[210:213], v160 offset:320
	ds_read_b128 v[214:217], v160 offset:384
	ds_read_b128 v[218:221], v160 offset:448
	ds_read_b32 v150, v164
	s_waitcnt lgkmcnt(9)
	v_and_b32_e32 v174, 0xfffff800, v169
	v_lshl_add_u64 v[176:177], v[172:173], 0, v[174:175]
	global_load_dwordx4 v[64:67], v[176:177], off
	global_load_dwordx4 v[68:71], v[176:177], off offset:64
	global_load_dwordx4 v[72:75], v[176:177], off offset:128
	global_load_dwordx4 v[76:79], v[176:177], off offset:192
	v_cndmask_b32_e64 v161, v234, v235, s[2:3]
	v_cndmask_b32_e64 v162, v236, v237, s[2:3]
	v_cvt_f32_i32_e32 v151, v151
	v_lshl_add_u32 v163, v149, 2, s50
	v_cndmask_b32_e64 v161, v161, v162, s[10:11]
	v_cvt_f32_i32_e32 v161, v161
	v_fmac_f32_e32 v161, 0xc0f00000, v151
	s_mov_b64 exec, s[12:13]
	ds_add_f32 v163, v161
	s_mov_b64 exec, -1
	s_waitcnt vmcnt(12)
	ds_bpermute_b32 v0, v171, v0
	ds_bpermute_b32 v1, v171, v1
	ds_bpermute_b32 v2, v171, v2
	ds_bpermute_b32 v3, v171, v3
	ds_bpermute_b32 v4, v171, v4
	ds_bpermute_b32 v5, v171, v5
	ds_bpermute_b32 v6, v171, v6
	ds_bpermute_b32 v7, v171, v7
	ds_bpermute_b32 v8, v171, v8
	ds_bpermute_b32 v9, v171, v9
	ds_bpermute_b32 v10, v171, v10
	ds_bpermute_b32 v11, v171, v11
	ds_bpermute_b32 v12, v171, v12
	ds_bpermute_b32 v13, v171, v13
	ds_bpermute_b32 v14, v171, v14
	ds_bpermute_b32 v15, v171, v15
	s_waitcnt lgkmcnt(12)
	v_and_b32_e32 v222, 0xf0f0f0f, v0
	v_and_b32_e32 v223, 0xf0f0f0f, v1
	v_and_b32_e32 v224, 0xf0f0f0f, v2
	v_and_b32_e32 v225, 0xf0f0f0f, v3
	v_lshrrev_b32_e32 v226, 4, v0
	v_lshrrev_b32_e32 v227, 4, v1
	v_lshrrev_b32_e32 v228, 4, v2
	v_lshrrev_b32_e32 v229, 4, v3
	v_and_b32_e32 v226, 0xf0f0f0f, v226
	v_and_b32_e32 v227, 0xf0f0f0f, v227
	v_and_b32_e32 v228, 0xf0f0f0f, v228
	v_and_b32_e32 v229, 0xf0f0f0f, v229
	v_mfma_i32_16x16x64_i8 v[230:233], v[222:225], v[190:193], 0
	s_nop 0
	v_mfma_i32_16x16x64_i8 v[230:233], v[226:229], v[194:197], v[230:233]
	s_waitcnt lgkmcnt(8)
	v_and_b32_e32 v222, 0xf0f0f0f, v4
	v_and_b32_e32 v223, 0xf0f0f0f, v5
	v_and_b32_e32 v224, 0xf0f0f0f, v6
	v_and_b32_e32 v225, 0xf0f0f0f, v7
	v_lshrrev_b32_e32 v226, 4, v4
	v_lshrrev_b32_e32 v227, 4, v5
	v_lshrrev_b32_e32 v228, 4, v6
	v_lshrrev_b32_e32 v229, 4, v7
	v_and_b32_e32 v226, 0xf0f0f0f, v226
	v_and_b32_e32 v227, 0xf0f0f0f, v227
	v_and_b32_e32 v228, 0xf0f0f0f, v228
	v_and_b32_e32 v229, 0xf0f0f0f, v229
	v_mfma_i32_16x16x64_i8 v[230:233], v[222:225], v[198:201], v[230:233]
	s_nop 0
	v_mfma_i32_16x16x64_i8 v[230:233], v[226:229], v[202:205], v[230:233]
	s_waitcnt lgkmcnt(4)
	v_and_b32_e32 v222, 0xf0f0f0f, v8
	v_and_b32_e32 v223, 0xf0f0f0f, v9
	v_and_b32_e32 v224, 0xf0f0f0f, v10
	v_and_b32_e32 v225, 0xf0f0f0f, v11
	v_lshrrev_b32_e32 v226, 4, v8
	v_lshrrev_b32_e32 v227, 4, v9
	v_lshrrev_b32_e32 v228, 4, v10
	v_lshrrev_b32_e32 v229, 4, v11
	v_and_b32_e32 v226, 0xf0f0f0f, v226
	v_and_b32_e32 v227, 0xf0f0f0f, v227
	v_and_b32_e32 v228, 0xf0f0f0f, v228
	v_and_b32_e32 v229, 0xf0f0f0f, v229
	v_mfma_i32_16x16x64_i8 v[230:233], v[222:225], v[206:209], v[230:233]
	s_nop 0
	v_mfma_i32_16x16x64_i8 v[230:233], v[226:229], v[210:213], v[230:233]
	s_waitcnt lgkmcnt(0)
	v_and_b32_e32 v222, 0xf0f0f0f, v12
	v_and_b32_e32 v223, 0xf0f0f0f, v13
	v_and_b32_e32 v224, 0xf0f0f0f, v14
	v_and_b32_e32 v225, 0xf0f0f0f, v15
	v_lshrrev_b32_e32 v226, 4, v12
	v_lshrrev_b32_e32 v227, 4, v13
	v_lshrrev_b32_e32 v228, 4, v14
	v_lshrrev_b32_e32 v229, 4, v15
	v_and_b32_e32 v226, 0xf0f0f0f, v226
	v_and_b32_e32 v227, 0xf0f0f0f, v227
	v_and_b32_e32 v228, 0xf0f0f0f, v228
	v_and_b32_e32 v229, 0xf0f0f0f, v229
	v_mfma_i32_16x16x64_i8 v[230:233], v[222:225], v[214:217], v[230:233]
	s_nop 0
	v_mfma_i32_16x16x64_i8 v[230:233], v[226:229], v[218:221], v[230:233]
	ds_read_b32 v182, v155 offset:256
	ds_read_b32 v166, v170 offset:256
	v_bfe_u32 v147, v183, 7, 4
	v_and_b32_e32 v149, 0x7ff, v183
	v_mad_u32_u24 v160, v147, s31, v154
	v_lshl_add_u32 v164, v147, 5, s16
	ds_read_b128 v[190:193], v160
	ds_read_b128 v[194:197], v160 offset:64
	ds_read_b128 v[198:201], v160 offset:128
	ds_read_b128 v[202:205], v160 offset:192
	ds_read_b128 v[206:209], v160 offset:256
	ds_read_b128 v[210:213], v160 offset:320
	ds_read_b128 v[214:217], v160 offset:384
	ds_read_b128 v[218:221], v160 offset:448
	ds_read_b32 v151, v164
	s_waitcnt lgkmcnt(9)
	v_and_b32_e32 v174, 0xfffff800, v166
	v_lshl_add_u64 v[176:177], v[172:173], 0, v[174:175]
	global_load_dwordx4 v[0:3], v[176:177], off
	global_load_dwordx4 v[4:7], v[176:177], off offset:64
	global_load_dwordx4 v[8:11], v[176:177], off offset:128
	global_load_dwordx4 v[12:15], v[176:177], off offset:192
	v_cndmask_b32_e64 v161, v230, v231, s[2:3]
	v_cndmask_b32_e64 v162, v232, v233, s[2:3]
	v_cvt_f32_i32_e32 v150, v150
	v_lshl_add_u32 v163, v148, 2, s50
	v_cndmask_b32_e64 v161, v161, v162, s[10:11]
	v_cvt_f32_i32_e32 v161, v161
	v_fmac_f32_e32 v161, 0xc0f00000, v150
	s_mov_b64 exec, s[12:13]
	ds_add_f32 v163, v161
	s_mov_b64 exec, -1
	s_waitcnt vmcnt(12)
	ds_bpermute_b32 v16, v171, v16
	ds_bpermute_b32 v17, v171, v17
	ds_bpermute_b32 v18, v171, v18
	ds_bpermute_b32 v19, v171, v19
	ds_bpermute_b32 v20, v171, v20
	ds_bpermute_b32 v21, v171, v21
	ds_bpermute_b32 v22, v171, v22
	ds_bpermute_b32 v23, v171, v23
	ds_bpermute_b32 v24, v171, v24
	ds_bpermute_b32 v25, v171, v25
	ds_bpermute_b32 v26, v171, v26
	ds_bpermute_b32 v27, v171, v27
	ds_bpermute_b32 v28, v171, v28
	ds_bpermute_b32 v29, v171, v29
	ds_bpermute_b32 v30, v171, v30
	ds_bpermute_b32 v31, v171, v31
	s_waitcnt lgkmcnt(12)
	v_and_b32_e32 v222, 0xf0f0f0f, v16
	v_and_b32_e32 v223, 0xf0f0f0f, v17
	v_and_b32_e32 v224, 0xf0f0f0f, v18
	v_and_b32_e32 v225, 0xf0f0f0f, v19
	v_lshrrev_b32_e32 v226, 4, v16
	v_lshrrev_b32_e32 v227, 4, v17
	v_lshrrev_b32_e32 v228, 4, v18
	v_lshrrev_b32_e32 v229, 4, v19
	v_and_b32_e32 v226, 0xf0f0f0f, v226
	v_and_b32_e32 v227, 0xf0f0f0f, v227
	v_and_b32_e32 v228, 0xf0f0f0f, v228
	v_and_b32_e32 v229, 0xf0f0f0f, v229
	v_mfma_i32_16x16x64_i8 v[234:237], v[222:225], v[190:193], 0
	s_nop 0
	v_mfma_i32_16x16x64_i8 v[234:237], v[226:229], v[194:197], v[234:237]
	s_waitcnt lgkmcnt(8)
	v_and_b32_e32 v222, 0xf0f0f0f, v20
	v_and_b32_e32 v223, 0xf0f0f0f, v21
	v_and_b32_e32 v224, 0xf0f0f0f, v22
	v_and_b32_e32 v225, 0xf0f0f0f, v23
	v_lshrrev_b32_e32 v226, 4, v20
	v_lshrrev_b32_e32 v227, 4, v21
	v_lshrrev_b32_e32 v228, 4, v22
	v_lshrrev_b32_e32 v229, 4, v23
	v_and_b32_e32 v226, 0xf0f0f0f, v226
	v_and_b32_e32 v227, 0xf0f0f0f, v227
	v_and_b32_e32 v228, 0xf0f0f0f, v228
	v_and_b32_e32 v229, 0xf0f0f0f, v229
	v_mfma_i32_16x16x64_i8 v[234:237], v[222:225], v[198:201], v[234:237]
	s_nop 0
	v_mfma_i32_16x16x64_i8 v[234:237], v[226:229], v[202:205], v[234:237]
	s_waitcnt lgkmcnt(4)
	v_and_b32_e32 v222, 0xf0f0f0f, v24
	v_and_b32_e32 v223, 0xf0f0f0f, v25
	v_and_b32_e32 v224, 0xf0f0f0f, v26
	v_and_b32_e32 v225, 0xf0f0f0f, v27
	v_lshrrev_b32_e32 v226, 4, v24
	v_lshrrev_b32_e32 v227, 4, v25
	v_lshrrev_b32_e32 v228, 4, v26
	v_lshrrev_b32_e32 v229, 4, v27
	v_and_b32_e32 v226, 0xf0f0f0f, v226
	v_and_b32_e32 v227, 0xf0f0f0f, v227
	v_and_b32_e32 v228, 0xf0f0f0f, v228
	v_and_b32_e32 v229, 0xf0f0f0f, v229
	v_mfma_i32_16x16x64_i8 v[234:237], v[222:225], v[206:209], v[234:237]
	s_nop 0
	v_mfma_i32_16x16x64_i8 v[234:237], v[226:229], v[210:213], v[234:237]
	s_waitcnt lgkmcnt(0)
	v_and_b32_e32 v222, 0xf0f0f0f, v28
	v_and_b32_e32 v223, 0xf0f0f0f, v29
	v_and_b32_e32 v224, 0xf0f0f0f, v30
	v_and_b32_e32 v225, 0xf0f0f0f, v31
	v_lshrrev_b32_e32 v226, 4, v28
	v_lshrrev_b32_e32 v227, 4, v29
	v_lshrrev_b32_e32 v228, 4, v30
	v_lshrrev_b32_e32 v229, 4, v31
	v_and_b32_e32 v226, 0xf0f0f0f, v226
	v_and_b32_e32 v227, 0xf0f0f0f, v227
	v_and_b32_e32 v228, 0xf0f0f0f, v228
	v_and_b32_e32 v229, 0xf0f0f0f, v229
	v_mfma_i32_16x16x64_i8 v[234:237], v[222:225], v[214:217], v[234:237]
	s_nop 0
	v_mfma_i32_16x16x64_i8 v[234:237], v[226:229], v[218:221], v[234:237]
	ds_read_b32 v183, v155 offset:320
	ds_read_b32 v167, v170 offset:320
	v_bfe_u32 v146, v184, 7, 4
	v_and_b32_e32 v148, 0x7ff, v184
	v_mad_u32_u24 v160, v146, s31, v154
	v_lshl_add_u32 v164, v146, 5, s16
	ds_read_b128 v[190:193], v160
	ds_read_b128 v[194:197], v160 offset:64
	ds_read_b128 v[198:201], v160 offset:128
	ds_read_b128 v[202:205], v160 offset:192
	ds_read_b128 v[206:209], v160 offset:256
	ds_read_b128 v[210:213], v160 offset:320
	ds_read_b128 v[214:217], v160 offset:384
	ds_read_b128 v[218:221], v160 offset:448
	ds_read_b32 v150, v164
	s_waitcnt lgkmcnt(9)
	v_and_b32_e32 v174, 0xfffff800, v167
	v_lshl_add_u64 v[176:177], v[172:173], 0, v[174:175]
	global_load_dwordx4 v[16:19], v[176:177], off
	global_load_dwordx4 v[20:23], v[176:177], off offset:64
	global_load_dwordx4 v[24:27], v[176:177], off offset:128
	global_load_dwordx4 v[28:31], v[176:177], off offset:192
	v_cndmask_b32_e64 v161, v234, v235, s[2:3]
	v_cndmask_b32_e64 v162, v236, v237, s[2:3]
	v_cvt_f32_i32_e32 v151, v151
	v_lshl_add_u32 v163, v149, 2, s50
	v_cndmask_b32_e64 v161, v161, v162, s[10:11]
	v_cvt_f32_i32_e32 v161, v161
	v_fmac_f32_e32 v161, 0xc0f00000, v151
	s_mov_b64 exec, s[12:13]
	ds_add_f32 v163, v161
	s_mov_b64 exec, -1
	s_waitcnt vmcnt(12)
	ds_bpermute_b32 v32, v171, v32
	ds_bpermute_b32 v33, v171, v33
	ds_bpermute_b32 v34, v171, v34
	ds_bpermute_b32 v35, v171, v35
	ds_bpermute_b32 v36, v171, v36
	ds_bpermute_b32 v37, v171, v37
	ds_bpermute_b32 v38, v171, v38
	ds_bpermute_b32 v39, v171, v39
	ds_bpermute_b32 v40, v171, v40
	ds_bpermute_b32 v41, v171, v41
	ds_bpermute_b32 v42, v171, v42
	ds_bpermute_b32 v43, v171, v43
	ds_bpermute_b32 v44, v171, v44
	ds_bpermute_b32 v45, v171, v45
	ds_bpermute_b32 v46, v171, v46
	ds_bpermute_b32 v47, v171, v47
	s_waitcnt lgkmcnt(12)
	v_and_b32_e32 v222, 0xf0f0f0f, v32
	v_and_b32_e32 v223, 0xf0f0f0f, v33
	v_and_b32_e32 v224, 0xf0f0f0f, v34
	v_and_b32_e32 v225, 0xf0f0f0f, v35
	v_lshrrev_b32_e32 v226, 4, v32
	v_lshrrev_b32_e32 v227, 4, v33
	v_lshrrev_b32_e32 v228, 4, v34
	v_lshrrev_b32_e32 v229, 4, v35
	v_and_b32_e32 v226, 0xf0f0f0f, v226
	v_and_b32_e32 v227, 0xf0f0f0f, v227
	v_and_b32_e32 v228, 0xf0f0f0f, v228
	v_and_b32_e32 v229, 0xf0f0f0f, v229
	v_mfma_i32_16x16x64_i8 v[230:233], v[222:225], v[190:193], 0
	s_nop 0
	v_mfma_i32_16x16x64_i8 v[230:233], v[226:229], v[194:197], v[230:233]
	s_waitcnt lgkmcnt(8)
	v_and_b32_e32 v222, 0xf0f0f0f, v36
	v_and_b32_e32 v223, 0xf0f0f0f, v37
	v_and_b32_e32 v224, 0xf0f0f0f, v38
	v_and_b32_e32 v225, 0xf0f0f0f, v39
	v_lshrrev_b32_e32 v226, 4, v36
	v_lshrrev_b32_e32 v227, 4, v37
	v_lshrrev_b32_e32 v228, 4, v38
	v_lshrrev_b32_e32 v229, 4, v39
	v_and_b32_e32 v226, 0xf0f0f0f, v226
	v_and_b32_e32 v227, 0xf0f0f0f, v227
	v_and_b32_e32 v228, 0xf0f0f0f, v228
	v_and_b32_e32 v229, 0xf0f0f0f, v229
	v_mfma_i32_16x16x64_i8 v[230:233], v[222:225], v[198:201], v[230:233]
	s_nop 0
	v_mfma_i32_16x16x64_i8 v[230:233], v[226:229], v[202:205], v[230:233]
	s_waitcnt lgkmcnt(4)
	v_and_b32_e32 v222, 0xf0f0f0f, v40
	v_and_b32_e32 v223, 0xf0f0f0f, v41
	v_and_b32_e32 v224, 0xf0f0f0f, v42
	v_and_b32_e32 v225, 0xf0f0f0f, v43
	v_lshrrev_b32_e32 v226, 4, v40
	v_lshrrev_b32_e32 v227, 4, v41
	v_lshrrev_b32_e32 v228, 4, v42
	v_lshrrev_b32_e32 v229, 4, v43
	v_and_b32_e32 v226, 0xf0f0f0f, v226
	v_and_b32_e32 v227, 0xf0f0f0f, v227
	v_and_b32_e32 v228, 0xf0f0f0f, v228
	v_and_b32_e32 v229, 0xf0f0f0f, v229
	v_mfma_i32_16x16x64_i8 v[230:233], v[222:225], v[206:209], v[230:233]
	s_nop 0
	v_mfma_i32_16x16x64_i8 v[230:233], v[226:229], v[210:213], v[230:233]
	s_waitcnt lgkmcnt(0)
	v_and_b32_e32 v222, 0xf0f0f0f, v44
	v_and_b32_e32 v223, 0xf0f0f0f, v45
	v_and_b32_e32 v224, 0xf0f0f0f, v46
	v_and_b32_e32 v225, 0xf0f0f0f, v47
	v_lshrrev_b32_e32 v226, 4, v44
	v_lshrrev_b32_e32 v227, 4, v45
	v_lshrrev_b32_e32 v228, 4, v46
	v_lshrrev_b32_e32 v229, 4, v47
	v_and_b32_e32 v226, 0xf0f0f0f, v226
	v_and_b32_e32 v227, 0xf0f0f0f, v227
	v_and_b32_e32 v228, 0xf0f0f0f, v228
	v_and_b32_e32 v229, 0xf0f0f0f, v229
	v_mfma_i32_16x16x64_i8 v[230:233], v[222:225], v[214:217], v[230:233]
	s_nop 0
	v_mfma_i32_16x16x64_i8 v[230:233], v[226:229], v[218:221], v[230:233]
	ds_read_b32 v184, v155 offset:384
	ds_read_b32 v168, v170 offset:384
	v_bfe_u32 v147, v185, 7, 4
	v_and_b32_e32 v149, 0x7ff, v185
	v_mad_u32_u24 v160, v147, s31, v154
	v_lshl_add_u32 v164, v147, 5, s16
	ds_read_b128 v[190:193], v160
	ds_read_b128 v[194:197], v160 offset:64
	ds_read_b128 v[198:201], v160 offset:128
	ds_read_b128 v[202:205], v160 offset:192
	ds_read_b128 v[206:209], v160 offset:256
	ds_read_b128 v[210:213], v160 offset:320
	ds_read_b128 v[214:217], v160 offset:384
	ds_read_b128 v[218:221], v160 offset:448
	ds_read_b32 v151, v164
	s_waitcnt lgkmcnt(9)
	v_and_b32_e32 v174, 0xfffff800, v168
	v_lshl_add_u64 v[176:177], v[172:173], 0, v[174:175]
	global_load_dwordx4 v[32:35], v[176:177], off
	global_load_dwordx4 v[36:39], v[176:177], off offset:64
	global_load_dwordx4 v[40:43], v[176:177], off offset:128
	global_load_dwordx4 v[44:47], v[176:177], off offset:192
	v_cndmask_b32_e64 v161, v230, v231, s[2:3]
	v_cndmask_b32_e64 v162, v232, v233, s[2:3]
	v_cvt_f32_i32_e32 v150, v150
	v_lshl_add_u32 v163, v148, 2, s50
	v_cndmask_b32_e64 v161, v161, v162, s[10:11]
	v_cvt_f32_i32_e32 v161, v161
	v_fmac_f32_e32 v161, 0xc0f00000, v150
	s_mov_b64 exec, s[12:13]
	ds_add_f32 v163, v161
	s_mov_b64 exec, -1
	s_waitcnt vmcnt(12)
	ds_bpermute_b32 v64, v171, v64
	ds_bpermute_b32 v65, v171, v65
	ds_bpermute_b32 v66, v171, v66
	ds_bpermute_b32 v67, v171, v67
	ds_bpermute_b32 v68, v171, v68
	ds_bpermute_b32 v69, v171, v69
	ds_bpermute_b32 v70, v171, v70
	ds_bpermute_b32 v71, v171, v71
	ds_bpermute_b32 v72, v171, v72
	ds_bpermute_b32 v73, v171, v73
	ds_bpermute_b32 v74, v171, v74
	ds_bpermute_b32 v75, v171, v75
	ds_bpermute_b32 v76, v171, v76
	ds_bpermute_b32 v77, v171, v77
	ds_bpermute_b32 v78, v171, v78
	ds_bpermute_b32 v79, v171, v79
	s_waitcnt lgkmcnt(12)
	v_and_b32_e32 v222, 0xf0f0f0f, v64
	v_and_b32_e32 v223, 0xf0f0f0f, v65
	v_and_b32_e32 v224, 0xf0f0f0f, v66
	v_and_b32_e32 v225, 0xf0f0f0f, v67
	v_lshrrev_b32_e32 v226, 4, v64
	v_lshrrev_b32_e32 v227, 4, v65
	v_lshrrev_b32_e32 v228, 4, v66
	v_lshrrev_b32_e32 v229, 4, v67
	v_and_b32_e32 v226, 0xf0f0f0f, v226
	v_and_b32_e32 v227, 0xf0f0f0f, v227
	v_and_b32_e32 v228, 0xf0f0f0f, v228
	v_and_b32_e32 v229, 0xf0f0f0f, v229
	v_mfma_i32_16x16x64_i8 v[234:237], v[222:225], v[190:193], 0
	s_nop 0
	v_mfma_i32_16x16x64_i8 v[234:237], v[226:229], v[194:197], v[234:237]
	s_waitcnt lgkmcnt(8)
	v_and_b32_e32 v222, 0xf0f0f0f, v68
	v_and_b32_e32 v223, 0xf0f0f0f, v69
	v_and_b32_e32 v224, 0xf0f0f0f, v70
	v_and_b32_e32 v225, 0xf0f0f0f, v71
	v_lshrrev_b32_e32 v226, 4, v68
	v_lshrrev_b32_e32 v227, 4, v69
	v_lshrrev_b32_e32 v228, 4, v70
	v_lshrrev_b32_e32 v229, 4, v71
	v_and_b32_e32 v226, 0xf0f0f0f, v226
	v_and_b32_e32 v227, 0xf0f0f0f, v227
	v_and_b32_e32 v228, 0xf0f0f0f, v228
	v_and_b32_e32 v229, 0xf0f0f0f, v229
	v_mfma_i32_16x16x64_i8 v[234:237], v[222:225], v[198:201], v[234:237]
	s_nop 0
	v_mfma_i32_16x16x64_i8 v[234:237], v[226:229], v[202:205], v[234:237]
	s_waitcnt lgkmcnt(4)
	v_and_b32_e32 v222, 0xf0f0f0f, v72
	v_and_b32_e32 v223, 0xf0f0f0f, v73
	v_and_b32_e32 v224, 0xf0f0f0f, v74
	v_and_b32_e32 v225, 0xf0f0f0f, v75
	v_lshrrev_b32_e32 v226, 4, v72
	v_lshrrev_b32_e32 v227, 4, v73
	v_lshrrev_b32_e32 v228, 4, v74
	v_lshrrev_b32_e32 v229, 4, v75
	v_and_b32_e32 v226, 0xf0f0f0f, v226
	v_and_b32_e32 v227, 0xf0f0f0f, v227
	v_and_b32_e32 v228, 0xf0f0f0f, v228
	v_and_b32_e32 v229, 0xf0f0f0f, v229
	v_mfma_i32_16x16x64_i8 v[234:237], v[222:225], v[206:209], v[234:237]
	s_nop 0
	v_mfma_i32_16x16x64_i8 v[234:237], v[226:229], v[210:213], v[234:237]
	s_waitcnt lgkmcnt(0)
	v_and_b32_e32 v222, 0xf0f0f0f, v76
	v_and_b32_e32 v223, 0xf0f0f0f, v77
	v_and_b32_e32 v224, 0xf0f0f0f, v78
	v_and_b32_e32 v225, 0xf0f0f0f, v79
	v_lshrrev_b32_e32 v226, 4, v76
	v_lshrrev_b32_e32 v227, 4, v77
	v_lshrrev_b32_e32 v228, 4, v78
	v_lshrrev_b32_e32 v229, 4, v79
	v_and_b32_e32 v226, 0xf0f0f0f, v226
	v_and_b32_e32 v227, 0xf0f0f0f, v227
	v_and_b32_e32 v228, 0xf0f0f0f, v228
	v_and_b32_e32 v229, 0xf0f0f0f, v229
	v_mfma_i32_16x16x64_i8 v[234:237], v[222:225], v[214:217], v[234:237]
	s_nop 0
	v_mfma_i32_16x16x64_i8 v[234:237], v[226:229], v[218:221], v[234:237]
	v_add_u32_e32 v155, 0x100, v155
	v_add_u32_e32 v170, 0x100, v170
	s_add_u32 s9, s9, 1
	s_cmp_lt_u32 s9, 31
	s_cbranch_scc1 .Lpu_loop
	ds_read_b32 v185, v155 offset:192
	ds_read_b32 v169, v170 offset:192
	v_bfe_u32 v146, v182, 7, 4
	v_and_b32_e32 v148, 0x7ff, v182
	v_mad_u32_u24 v160, v146, s31, v154
	v_lshl_add_u32 v164, v146, 5, s16
	ds_read_b128 v[190:193], v160
	ds_read_b128 v[194:197], v160 offset:64
	ds_read_b128 v[198:201], v160 offset:128
	ds_read_b128 v[202:205], v160 offset:192
	ds_read_b128 v[206:209], v160 offset:256
	ds_read_b128 v[210:213], v160 offset:320
	ds_read_b128 v[214:217], v160 offset:384
	ds_read_b128 v[218:221], v160 offset:448
	ds_read_b32 v150, v164
	s_waitcnt lgkmcnt(9)
	v_and_b32_e32 v174, 0xfffff800, v169
	v_lshl_add_u64 v[176:177], v[172:173], 0, v[174:175]
	global_load_dwordx4 v[64:67], v[176:177], off
	global_load_dwordx4 v[68:71], v[176:177], off offset:64
	global_load_dwordx4 v[72:75], v[176:177], off offset:128
	global_load_dwordx4 v[76:79], v[176:177], off offset:192
	v_cndmask_b32_e64 v161, v234, v235, s[2:3]
	v_cndmask_b32_e64 v162, v236, v237, s[2:3]
	v_cvt_f32_i32_e32 v151, v151
	v_lshl_add_u32 v163, v149, 2, s50
	v_cndmask_b32_e64 v161, v161, v162, s[10:11]
	v_cvt_f32_i32_e32 v161, v161
	v_fmac_f32_e32 v161, 0xc0f00000, v151
	s_mov_b64 exec, s[12:13]
	ds_add_f32 v163, v161
	s_mov_b64 exec, -1
	s_waitcnt vmcnt(12)
	ds_bpermute_b32 v0, v171, v0
	ds_bpermute_b32 v1, v171, v1
	ds_bpermute_b32 v2, v171, v2
	ds_bpermute_b32 v3, v171, v3
	ds_bpermute_b32 v4, v171, v4
	ds_bpermute_b32 v5, v171, v5
	ds_bpermute_b32 v6, v171, v6
	ds_bpermute_b32 v7, v171, v7
	ds_bpermute_b32 v8, v171, v8
	ds_bpermute_b32 v9, v171, v9
	ds_bpermute_b32 v10, v171, v10
	ds_bpermute_b32 v11, v171, v11
	ds_bpermute_b32 v12, v171, v12
	ds_bpermute_b32 v13, v171, v13
	ds_bpermute_b32 v14, v171, v14
	ds_bpermute_b32 v15, v171, v15
	s_waitcnt lgkmcnt(12)
	v_and_b32_e32 v222, 0xf0f0f0f, v0
	v_and_b32_e32 v223, 0xf0f0f0f, v1
	v_and_b32_e32 v224, 0xf0f0f0f, v2
	v_and_b32_e32 v225, 0xf0f0f0f, v3
	v_lshrrev_b32_e32 v226, 4, v0
	v_lshrrev_b32_e32 v227, 4, v1
	v_lshrrev_b32_e32 v228, 4, v2
	v_lshrrev_b32_e32 v229, 4, v3
	v_and_b32_e32 v226, 0xf0f0f0f, v226
	v_and_b32_e32 v227, 0xf0f0f0f, v227
	v_and_b32_e32 v228, 0xf0f0f0f, v228
	v_and_b32_e32 v229, 0xf0f0f0f, v229
	v_mfma_i32_16x16x64_i8 v[230:233], v[222:225], v[190:193], 0
	s_nop 0
	v_mfma_i32_16x16x64_i8 v[230:233], v[226:229], v[194:197], v[230:233]
	s_waitcnt lgkmcnt(8)
	v_and_b32_e32 v222, 0xf0f0f0f, v4
	v_and_b32_e32 v223, 0xf0f0f0f, v5
	v_and_b32_e32 v224, 0xf0f0f0f, v6
	v_and_b32_e32 v225, 0xf0f0f0f, v7
	v_lshrrev_b32_e32 v226, 4, v4
	v_lshrrev_b32_e32 v227, 4, v5
	v_lshrrev_b32_e32 v228, 4, v6
	v_lshrrev_b32_e32 v229, 4, v7
	v_and_b32_e32 v226, 0xf0f0f0f, v226
	v_and_b32_e32 v227, 0xf0f0f0f, v227
	v_and_b32_e32 v228, 0xf0f0f0f, v228
	v_and_b32_e32 v229, 0xf0f0f0f, v229
	v_mfma_i32_16x16x64_i8 v[230:233], v[222:225], v[198:201], v[230:233]
	s_nop 0
	v_mfma_i32_16x16x64_i8 v[230:233], v[226:229], v[202:205], v[230:233]
	s_waitcnt lgkmcnt(4)
	v_and_b32_e32 v222, 0xf0f0f0f, v8
	v_and_b32_e32 v223, 0xf0f0f0f, v9
	v_and_b32_e32 v224, 0xf0f0f0f, v10
	v_and_b32_e32 v225, 0xf0f0f0f, v11
	v_lshrrev_b32_e32 v226, 4, v8
	v_lshrrev_b32_e32 v227, 4, v9
	v_lshrrev_b32_e32 v228, 4, v10
	v_lshrrev_b32_e32 v229, 4, v11
	v_and_b32_e32 v226, 0xf0f0f0f, v226
	v_and_b32_e32 v227, 0xf0f0f0f, v227
	v_and_b32_e32 v228, 0xf0f0f0f, v228
	v_and_b32_e32 v229, 0xf0f0f0f, v229
	v_mfma_i32_16x16x64_i8 v[230:233], v[222:225], v[206:209], v[230:233]
	s_nop 0
	v_mfma_i32_16x16x64_i8 v[230:233], v[226:229], v[210:213], v[230:233]
	s_waitcnt lgkmcnt(0)
	v_and_b32_e32 v222, 0xf0f0f0f, v12
	v_and_b32_e32 v223, 0xf0f0f0f, v13
	v_and_b32_e32 v224, 0xf0f0f0f, v14
	v_and_b32_e32 v225, 0xf0f0f0f, v15
	v_lshrrev_b32_e32 v226, 4, v12
	v_lshrrev_b32_e32 v227, 4, v13
	v_lshrrev_b32_e32 v228, 4, v14
	v_lshrrev_b32_e32 v229, 4, v15
	v_and_b32_e32 v226, 0xf0f0f0f, v226
	v_and_b32_e32 v227, 0xf0f0f0f, v227
	v_and_b32_e32 v228, 0xf0f0f0f, v228
	v_and_b32_e32 v229, 0xf0f0f0f, v229
	v_mfma_i32_16x16x64_i8 v[230:233], v[222:225], v[214:217], v[230:233]
	s_nop 0
	v_mfma_i32_16x16x64_i8 v[230:233], v[226:229], v[218:221], v[230:233]
	v_bfe_u32 v147, v183, 7, 4
	v_and_b32_e32 v149, 0x7ff, v183
	v_mad_u32_u24 v160, v147, s31, v154
	v_lshl_add_u32 v164, v147, 5, s16
	ds_read_b128 v[190:193], v160
	ds_read_b128 v[194:197], v160 offset:64
	ds_read_b128 v[198:201], v160 offset:128
	ds_read_b128 v[202:205], v160 offset:192
	ds_read_b128 v[206:209], v160 offset:256
	ds_read_b128 v[210:213], v160 offset:320
	ds_read_b128 v[214:217], v160 offset:384
	ds_read_b128 v[218:221], v160 offset:448
	ds_read_b32 v151, v164
	s_waitcnt lgkmcnt(9)
	v_cndmask_b32_e64 v161, v230, v231, s[2:3]
	v_cndmask_b32_e64 v162, v232, v233, s[2:3]
	v_cvt_f32_i32_e32 v150, v150
	v_lshl_add_u32 v163, v148, 2, s50
	v_cndmask_b32_e64 v161, v161, v162, s[10:11]
	v_cvt_f32_i32_e32 v161, v161
	v_fmac_f32_e32 v161, 0xc0f00000, v150
	s_mov_b64 exec, s[12:13]
	ds_add_f32 v163, v161
	s_mov_b64 exec, -1
	s_waitcnt vmcnt(8)
	ds_bpermute_b32 v16, v171, v16
	ds_bpermute_b32 v17, v171, v17
	ds_bpermute_b32 v18, v171, v18
	ds_bpermute_b32 v19, v171, v19
	ds_bpermute_b32 v20, v171, v20
	ds_bpermute_b32 v21, v171, v21
	ds_bpermute_b32 v22, v171, v22
	ds_bpermute_b32 v23, v171, v23
	ds_bpermute_b32 v24, v171, v24
	ds_bpermute_b32 v25, v171, v25
	ds_bpermute_b32 v26, v171, v26
	ds_bpermute_b32 v27, v171, v27
	ds_bpermute_b32 v28, v171, v28
	ds_bpermute_b32 v29, v171, v29
	ds_bpermute_b32 v30, v171, v30
	ds_bpermute_b32 v31, v171, v31
	s_waitcnt lgkmcnt(12)
	v_and_b32_e32 v222, 0xf0f0f0f, v16
	v_and_b32_e32 v223, 0xf0f0f0f, v17
	v_and_b32_e32 v224, 0xf0f0f0f, v18
	v_and_b32_e32 v225, 0xf0f0f0f, v19
	v_lshrrev_b32_e32 v226, 4, v16
	v_lshrrev_b32_e32 v227, 4, v17
	v_lshrrev_b32_e32 v228, 4, v18
	v_lshrrev_b32_e32 v229, 4, v19
	v_and_b32_e32 v226, 0xf0f0f0f, v226
	v_and_b32_e32 v227, 0xf0f0f0f, v227
	v_and_b32_e32 v228, 0xf0f0f0f, v228
	v_and_b32_e32 v229, 0xf0f0f0f, v229
	v_mfma_i32_16x16x64_i8 v[234:237], v[222:225], v[190:193], 0
	s_nop 0
	v_mfma_i32_16x16x64_i8 v[234:237], v[226:229], v[194:197], v[234:237]
	s_waitcnt lgkmcnt(8)
	v_and_b32_e32 v222, 0xf0f0f0f, v20
	v_and_b32_e32 v223, 0xf0f0f0f, v21
	v_and_b32_e32 v224, 0xf0f0f0f, v22
	v_and_b32_e32 v225, 0xf0f0f0f, v23
	v_lshrrev_b32_e32 v226, 4, v20
	v_lshrrev_b32_e32 v227, 4, v21
	v_lshrrev_b32_e32 v228, 4, v22
	v_lshrrev_b32_e32 v229, 4, v23
	v_and_b32_e32 v226, 0xf0f0f0f, v226
	v_and_b32_e32 v227, 0xf0f0f0f, v227
	v_and_b32_e32 v228, 0xf0f0f0f, v228
	v_and_b32_e32 v229, 0xf0f0f0f, v229
	v_mfma_i32_16x16x64_i8 v[234:237], v[222:225], v[198:201], v[234:237]
	s_nop 0
	v_mfma_i32_16x16x64_i8 v[234:237], v[226:229], v[202:205], v[234:237]
	s_waitcnt lgkmcnt(4)
	v_and_b32_e32 v222, 0xf0f0f0f, v24
	v_and_b32_e32 v223, 0xf0f0f0f, v25
	v_and_b32_e32 v224, 0xf0f0f0f, v26
	v_and_b32_e32 v225, 0xf0f0f0f, v27
	v_lshrrev_b32_e32 v226, 4, v24
	v_lshrrev_b32_e32 v227, 4, v25
	v_lshrrev_b32_e32 v228, 4, v26
	v_lshrrev_b32_e32 v229, 4, v27
	v_and_b32_e32 v226, 0xf0f0f0f, v226
	v_and_b32_e32 v227, 0xf0f0f0f, v227
	v_and_b32_e32 v228, 0xf0f0f0f, v228
	v_and_b32_e32 v229, 0xf0f0f0f, v229
	v_mfma_i32_16x16x64_i8 v[234:237], v[222:225], v[206:209], v[234:237]
	s_nop 0
	v_mfma_i32_16x16x64_i8 v[234:237], v[226:229], v[210:213], v[234:237]
	s_waitcnt lgkmcnt(0)
	v_and_b32_e32 v222, 0xf0f0f0f, v28
	v_and_b32_e32 v223, 0xf0f0f0f, v29
	v_and_b32_e32 v224, 0xf0f0f0f, v30
	v_and_b32_e32 v225, 0xf0f0f0f, v31
	v_lshrrev_b32_e32 v226, 4, v28
	v_lshrrev_b32_e32 v227, 4, v29
	v_lshrrev_b32_e32 v228, 4, v30
	v_lshrrev_b32_e32 v229, 4, v31
	v_and_b32_e32 v226, 0xf0f0f0f, v226
	v_and_b32_e32 v227, 0xf0f0f0f, v227
	v_and_b32_e32 v228, 0xf0f0f0f, v228
	v_and_b32_e32 v229, 0xf0f0f0f, v229
	v_mfma_i32_16x16x64_i8 v[234:237], v[222:225], v[214:217], v[234:237]
	s_nop 0
	v_mfma_i32_16x16x64_i8 v[234:237], v[226:229], v[218:221], v[234:237]
	v_bfe_u32 v146, v184, 7, 4
	v_and_b32_e32 v148, 0x7ff, v184
	v_mad_u32_u24 v160, v146, s31, v154
	v_lshl_add_u32 v164, v146, 5, s16
	ds_read_b128 v[190:193], v160
	ds_read_b128 v[194:197], v160 offset:64
	ds_read_b128 v[198:201], v160 offset:128
	ds_read_b128 v[202:205], v160 offset:192
	ds_read_b128 v[206:209], v160 offset:256
	ds_read_b128 v[210:213], v160 offset:320
	ds_read_b128 v[214:217], v160 offset:384
	ds_read_b128 v[218:221], v160 offset:448
	ds_read_b32 v150, v164
	s_waitcnt lgkmcnt(9)
	v_cndmask_b32_e64 v161, v234, v235, s[2:3]
	v_cndmask_b32_e64 v162, v236, v237, s[2:3]
	v_cvt_f32_i32_e32 v151, v151
	v_lshl_add_u32 v163, v149, 2, s50
	v_cndmask_b32_e64 v161, v161, v162, s[10:11]
	v_cvt_f32_i32_e32 v161, v161
	v_fmac_f32_e32 v161, 0xc0f00000, v151
	s_mov_b64 exec, s[12:13]
	ds_add_f32 v163, v161
	s_mov_b64 exec, -1
	s_waitcnt vmcnt(4)
	ds_bpermute_b32 v32, v171, v32
	ds_bpermute_b32 v33, v171, v33
	ds_bpermute_b32 v34, v171, v34
	ds_bpermute_b32 v35, v171, v35
	ds_bpermute_b32 v36, v171, v36
	ds_bpermute_b32 v37, v171, v37
	ds_bpermute_b32 v38, v171, v38
	ds_bpermute_b32 v39, v171, v39
	ds_bpermute_b32 v40, v171, v40
	ds_bpermute_b32 v41, v171, v41
	ds_bpermute_b32 v42, v171, v42
	ds_bpermute_b32 v43, v171, v43
	ds_bpermute_b32 v44, v171, v44
	ds_bpermute_b32 v45, v171, v45
	ds_bpermute_b32 v46, v171, v46
	ds_bpermute_b32 v47, v171, v47
	s_waitcnt lgkmcnt(12)
	v_and_b32_e32 v222, 0xf0f0f0f, v32
	v_and_b32_e32 v223, 0xf0f0f0f, v33
	v_and_b32_e32 v224, 0xf0f0f0f, v34
	v_and_b32_e32 v225, 0xf0f0f0f, v35
	v_lshrrev_b32_e32 v226, 4, v32
	v_lshrrev_b32_e32 v227, 4, v33
	v_lshrrev_b32_e32 v228, 4, v34
	v_lshrrev_b32_e32 v229, 4, v35
	v_and_b32_e32 v226, 0xf0f0f0f, v226
	v_and_b32_e32 v227, 0xf0f0f0f, v227
	v_and_b32_e32 v228, 0xf0f0f0f, v228
	v_and_b32_e32 v229, 0xf0f0f0f, v229
	v_mfma_i32_16x16x64_i8 v[230:233], v[222:225], v[190:193], 0
	s_nop 0
	v_mfma_i32_16x16x64_i8 v[230:233], v[226:229], v[194:197], v[230:233]
	s_waitcnt lgkmcnt(8)
	v_and_b32_e32 v222, 0xf0f0f0f, v36
	v_and_b32_e32 v223, 0xf0f0f0f, v37
	v_and_b32_e32 v224, 0xf0f0f0f, v38
	v_and_b32_e32 v225, 0xf0f0f0f, v39
	v_lshrrev_b32_e32 v226, 4, v36
	v_lshrrev_b32_e32 v227, 4, v37
	v_lshrrev_b32_e32 v228, 4, v38
	v_lshrrev_b32_e32 v229, 4, v39
	v_and_b32_e32 v226, 0xf0f0f0f, v226
	v_and_b32_e32 v227, 0xf0f0f0f, v227
	v_and_b32_e32 v228, 0xf0f0f0f, v228
	v_and_b32_e32 v229, 0xf0f0f0f, v229
	v_mfma_i32_16x16x64_i8 v[230:233], v[222:225], v[198:201], v[230:233]
	s_nop 0
	v_mfma_i32_16x16x64_i8 v[230:233], v[226:229], v[202:205], v[230:233]
	s_waitcnt lgkmcnt(4)
	v_and_b32_e32 v222, 0xf0f0f0f, v40
	v_and_b32_e32 v223, 0xf0f0f0f, v41
	v_and_b32_e32 v224, 0xf0f0f0f, v42
	v_and_b32_e32 v225, 0xf0f0f0f, v43
	v_lshrrev_b32_e32 v226, 4, v40
	v_lshrrev_b32_e32 v227, 4, v41
	v_lshrrev_b32_e32 v228, 4, v42
	v_lshrrev_b32_e32 v229, 4, v43
	v_and_b32_e32 v226, 0xf0f0f0f, v226
	v_and_b32_e32 v227, 0xf0f0f0f, v227
	v_and_b32_e32 v228, 0xf0f0f0f, v228
	v_and_b32_e32 v229, 0xf0f0f0f, v229
	v_mfma_i32_16x16x64_i8 v[230:233], v[222:225], v[206:209], v[230:233]
	s_nop 0
	v_mfma_i32_16x16x64_i8 v[230:233], v[226:229], v[210:213], v[230:233]
	s_waitcnt lgkmcnt(0)
	v_and_b32_e32 v222, 0xf0f0f0f, v44
	v_and_b32_e32 v223, 0xf0f0f0f, v45
	v_and_b32_e32 v224, 0xf0f0f0f, v46
	v_and_b32_e32 v225, 0xf0f0f0f, v47
	v_lshrrev_b32_e32 v226, 4, v44
	v_lshrrev_b32_e32 v227, 4, v45
	v_lshrrev_b32_e32 v228, 4, v46
	v_lshrrev_b32_e32 v229, 4, v47
	v_and_b32_e32 v226, 0xf0f0f0f, v226
	v_and_b32_e32 v227, 0xf0f0f0f, v227
	v_and_b32_e32 v228, 0xf0f0f0f, v228
	v_and_b32_e32 v229, 0xf0f0f0f, v229
	v_mfma_i32_16x16x64_i8 v[230:233], v[222:225], v[214:217], v[230:233]
	s_nop 0
	v_mfma_i32_16x16x64_i8 v[230:233], v[226:229], v[218:221], v[230:233]
	v_bfe_u32 v147, v185, 7, 4
	v_and_b32_e32 v149, 0x7ff, v185
	v_mad_u32_u24 v160, v147, s31, v154
	v_lshl_add_u32 v164, v147, 5, s16
	ds_read_b128 v[190:193], v160
	ds_read_b128 v[194:197], v160 offset:64
	ds_read_b128 v[198:201], v160 offset:128
	ds_read_b128 v[202:205], v160 offset:192
	ds_read_b128 v[206:209], v160 offset:256
	ds_read_b128 v[210:213], v160 offset:320
	ds_read_b128 v[214:217], v160 offset:384
	ds_read_b128 v[218:221], v160 offset:448
	ds_read_b32 v151, v164
	s_waitcnt lgkmcnt(9)
	v_cndmask_b32_e64 v161, v230, v231, s[2:3]
	v_cndmask_b32_e64 v162, v232, v233, s[2:3]
	v_cvt_f32_i32_e32 v150, v150
	v_lshl_add_u32 v163, v148, 2, s50
	v_cndmask_b32_e64 v161, v161, v162, s[10:11]
	v_cvt_f32_i32_e32 v161, v161
	v_fmac_f32_e32 v161, 0xc0f00000, v150
	s_mov_b64 exec, s[12:13]
	ds_add_f32 v163, v161
	s_mov_b64 exec, -1
	s_waitcnt vmcnt(0)
	ds_bpermute_b32 v64, v171, v64
	ds_bpermute_b32 v65, v171, v65
	ds_bpermute_b32 v66, v171, v66
	ds_bpermute_b32 v67, v171, v67
	ds_bpermute_b32 v68, v171, v68
	ds_bpermute_b32 v69, v171, v69
	ds_bpermute_b32 v70, v171, v70
	ds_bpermute_b32 v71, v171, v71
	ds_bpermute_b32 v72, v171, v72
	ds_bpermute_b32 v73, v171, v73
	ds_bpermute_b32 v74, v171, v74
	ds_bpermute_b32 v75, v171, v75
	ds_bpermute_b32 v76, v171, v76
	ds_bpermute_b32 v77, v171, v77
	ds_bpermute_b32 v78, v171, v78
	ds_bpermute_b32 v79, v171, v79
	s_waitcnt lgkmcnt(12)
	v_and_b32_e32 v222, 0xf0f0f0f, v64
	v_and_b32_e32 v223, 0xf0f0f0f, v65
	v_and_b32_e32 v224, 0xf0f0f0f, v66
	v_and_b32_e32 v225, 0xf0f0f0f, v67
	v_lshrrev_b32_e32 v226, 4, v64
	v_lshrrev_b32_e32 v227, 4, v65
	v_lshrrev_b32_e32 v228, 4, v66
	v_lshrrev_b32_e32 v229, 4, v67
	v_and_b32_e32 v226, 0xf0f0f0f, v226
	v_and_b32_e32 v227, 0xf0f0f0f, v227
	v_and_b32_e32 v228, 0xf0f0f0f, v228
	v_and_b32_e32 v229, 0xf0f0f0f, v229
	v_mfma_i32_16x16x64_i8 v[234:237], v[222:225], v[190:193], 0
	s_nop 0
	v_mfma_i32_16x16x64_i8 v[234:237], v[226:229], v[194:197], v[234:237]
	s_waitcnt lgkmcnt(8)
	v_and_b32_e32 v222, 0xf0f0f0f, v68
	v_and_b32_e32 v223, 0xf0f0f0f, v69
	v_and_b32_e32 v224, 0xf0f0f0f, v70
	v_and_b32_e32 v225, 0xf0f0f0f, v71
	v_lshrrev_b32_e32 v226, 4, v68
	v_lshrrev_b32_e32 v227, 4, v69
	v_lshrrev_b32_e32 v228, 4, v70
	v_lshrrev_b32_e32 v229, 4, v71
	v_and_b32_e32 v226, 0xf0f0f0f, v226
	v_and_b32_e32 v227, 0xf0f0f0f, v227
	v_and_b32_e32 v228, 0xf0f0f0f, v228
	v_and_b32_e32 v229, 0xf0f0f0f, v229
	v_mfma_i32_16x16x64_i8 v[234:237], v[222:225], v[198:201], v[234:237]
	s_nop 0
	v_mfma_i32_16x16x64_i8 v[234:237], v[226:229], v[202:205], v[234:237]
	s_waitcnt lgkmcnt(4)
	v_and_b32_e32 v222, 0xf0f0f0f, v72
	v_and_b32_e32 v223, 0xf0f0f0f, v73
	v_and_b32_e32 v224, 0xf0f0f0f, v74
	v_and_b32_e32 v225, 0xf0f0f0f, v75
	v_lshrrev_b32_e32 v226, 4, v72
	v_lshrrev_b32_e32 v227, 4, v73
	v_lshrrev_b32_e32 v228, 4, v74
	v_lshrrev_b32_e32 v229, 4, v75
	v_and_b32_e32 v226, 0xf0f0f0f, v226
	v_and_b32_e32 v227, 0xf0f0f0f, v227
	v_and_b32_e32 v228, 0xf0f0f0f, v228
	v_and_b32_e32 v229, 0xf0f0f0f, v229
	v_mfma_i32_16x16x64_i8 v[234:237], v[222:225], v[206:209], v[234:237]
	s_nop 0
	v_mfma_i32_16x16x64_i8 v[234:237], v[226:229], v[210:213], v[234:237]
	s_waitcnt lgkmcnt(0)
	v_and_b32_e32 v222, 0xf0f0f0f, v76
	v_and_b32_e32 v223, 0xf0f0f0f, v77
	v_and_b32_e32 v224, 0xf0f0f0f, v78
	v_and_b32_e32 v225, 0xf0f0f0f, v79
	v_lshrrev_b32_e32 v226, 4, v76
	v_lshrrev_b32_e32 v227, 4, v77
	v_lshrrev_b32_e32 v228, 4, v78
	v_lshrrev_b32_e32 v229, 4, v79
	v_and_b32_e32 v226, 0xf0f0f0f, v226
	v_and_b32_e32 v227, 0xf0f0f0f, v227
	v_and_b32_e32 v228, 0xf0f0f0f, v228
	v_and_b32_e32 v229, 0xf0f0f0f, v229
	v_mfma_i32_16x16x64_i8 v[234:237], v[222:225], v[214:217], v[234:237]
	s_nop 0
	v_mfma_i32_16x16x64_i8 v[234:237], v[226:229], v[218:221], v[234:237]
	s_waitcnt lgkmcnt(0)
	s_nop 7
	v_cndmask_b32_e64 v161, v234, v235, s[2:3]
	v_cndmask_b32_e64 v162, v236, v237, s[2:3]
	v_cvt_f32_i32_e32 v151, v151
	v_lshl_add_u32 v163, v149, 2, s50
	v_cndmask_b32_e64 v161, v161, v162, s[10:11]
	v_cvt_f32_i32_e32 v161, v161
	v_fmac_f32_e32 v161, 0xc0f00000, v151
	s_mov_b64 exec, s[12:13]
	ds_add_f32 v163, v161
	s_mov_b64 exec, -1
	s_waitcnt lgkmcnt(0)
	s_barrier
	s_nop 2
	ds_read_b32 v0, v54
	v_ashrrev_i32_e32 v1, 7, v50
	v_lshl_add_u32 v1, v1, 2, 0
	v_add_u32_e32 v1, 0x20900, v1
	ds_read_b32 v2, v1
	ds_read_b32 v3, v51
	s_waitcnt lgkmcnt(2)
	v_ashrrev_i32_e32 v1, 31, v0
	v_lshl_add_u64 v[0:1], v[0:1], 2, s[74:75]
	global_load_dword v4, v[0:1], off
	s_waitcnt lgkmcnt(0)
	v_mul_f32_e32 v2, v3, v2
	s_waitcnt vmcnt(0)
	v_mul_f32_e32 v3, v2, v4
	v_mul_f32_e32 v4, 0x3f3504f3, v3
	v_cmp_nlt_f32_e64 s[0:1], |v4|, 1.0
	s_and_saveexec_b64 s[2:3], s[0:1]
	s_xor_b64 s[0:1], exec, s[2:3]
	s_cbranch_execz .LBB0_1569
	v_fma_f32 v2, |v4|, s37, v143
	v_fma_f32 v2, |v4|, v2, s38
	v_fma_f32 v2, |v4|, v2, s39
	v_fma_f32 v2, |v4|, v2, s40
	v_fma_f32 v2, |v4|, v2, s41
	v_fma_f32 v2, |v4|, v2, s42
	v_fma_f32 v2, |v4|, v2, |v4|
	v_mul_f32_e32 v5, 0xbfb8aa3b, v2
	v_fma_f32 v6, v2, s43, -v5
	v_rndne_f32_e32 v7, v5
	v_fmac_f32_e32 v6, 0xb2a5705f, v2
	v_sub_f32_e32 v5, v5, v7
	v_add_f32_e32 v5, v5, v6
	v_cvt_i32_f32_e32 v6, v7
	v_exp_f32_e32 v5, v5
	v_cmp_nlt_f32_e32 vcc, s44, v2
	v_ldexp_f32 v5, v5, v6
	s_nop 0
	v_cndmask_b32_e32 v5, 0, v5, vcc
	v_cmp_ngt_f32_e32 vcc, s45, v2
	s_nop 1
	v_cndmask_b32_e32 v2, v144, v5, vcc
	v_sub_f32_e32 v5, 1.0, v2
